# v20 + P5 pass: the mixer-output rows (each 128-B line is touched by two loads) loaded through L1 (plain) instead of nt
# speedup vs baseline: 1.0137x; 1.0010x over previous
; #define YQ_XLOAD(P) do { _Pragma("unroll") for (int u = 0; u < 2; ++u) { const bf16* xr = F.HA + (size_t)(tb + F.wave * 8 + 2 * (P) + u) * D + 16 * lane; \
;             _Pragma("unroll") for (int jj = 0; jj < 2; ++jj) _Pragma("unroll") for (int q = 0; q < 2; ++q) xn[u][2 * jj + q] = __builtin_nontemporal_load((const GAS v4u*)(xr + 1024 * jj + 8 * q)); } } while (0)
; DI void yq_pass(Frame& F) {
;     ...
;     for (int tb = (int)blockIdx.x * 64; tb < M; tb += F.G * 64) {
;         v4u xn[2][4];
;     ...
;         YQ_XLOAD(0);
.LBB0_899:
	s_add_i32 s2, s12, s14
	s_ashr_i32 s3, s2, 31
	s_lshl_b64 s[10:11], s[2:3], 12
	s_or_b32 s2, s2, 1
	s_ashr_i32 s3, s2, 31
	v_lshl_add_u64 v[2:3], v[66:67], 0, s[10:11]
	s_lshl_b64 s[2:3], s[2:3], 12
	global_load_dwordx4 v[38:41], v[2:3], off offset:16
	global_load_dwordx4 v[54:57], v[2:3], off
	global_load_dwordx4 v[34:37], v[2:3], off offset:2064
	global_load_dwordx4 v[50:53], v[2:3], off offset:2048
	v_lshl_add_u64 v[2:3], v[66:67], 0, s[2:3]
	global_load_dwordx4 v[62:65], v[2:3], off
	global_load_dwordx4 v[46:49], v[2:3], off offset:16
	global_load_dwordx4 v[58:61], v[2:3], off offset:2048
	global_load_dwordx4 v[42:45], v[2:3], off offset:2064
	s_or_b32 s28, s12, 1
	s_mov_b32 s29, 0
	s_waitcnt vmcnt(7)
	v_mov_b64_e32 v[6:7], v[38:39]
	s_waitcnt vmcnt(6)
	v_mov_b64_e32 v[2:3], v[54:55]
	s_waitcnt vmcnt(5)
	v_mov_b64_e32 v[14:15], v[34:35]
	s_waitcnt vmcnt(4)
	v_mov_b64_e32 v[10:11], v[50:51]
	s_waitcnt vmcnt(3)
	v_mov_b64_e32 v[18:19], v[62:63]
	s_waitcnt vmcnt(2)
	v_mov_b64_e32 v[22:23], v[46:47]
	s_waitcnt vmcnt(1)
	v_mov_b64_e32 v[26:27], v[58:59]
	s_waitcnt vmcnt(0)
	v_mov_b64_e32 v[30:31], v[42:43]
	v_mov_b64_e32 v[4:5], v[56:57]
	v_mov_b64_e32 v[8:9], v[40:41]
	v_mov_b64_e32 v[12:13], v[52:53]
	v_mov_b64_e32 v[16:17], v[36:37]
	v_mov_b64_e32 v[20:21], v[64:65]
	v_mov_b64_e32 v[24:25], v[48:49]
	v_mov_b64_e32 v[28:29], v[60:61]
	v_mov_b64_e32 v[32:33], v[44:45]
	s_branch .LBB0_901

; #define YQ_XLOAD(P) do { _Pragma("unroll") for (int u = 0; u < 2; ++u) { const bf16* xr = F.HA + (size_t)(tb + F.wave * 8 + 2 * (P) + u) * D + 16 * lane; \
;             _Pragma("unroll") for (int jj = 0; jj < 2; ++jj) _Pragma("unroll") for (int q = 0; q < 2; ++q) xn[u][2 * jj + q] = __builtin_nontemporal_load((const GAS v4u*)(xr + 1024 * jj + 8 * q)); } } while (0)
; DI void yq_pass(Frame& F) {
;     ...
;         YQ_XLOAD(0);
; #pragma unroll 1
;         for (int p = 0; p < 4; ++p) {
;             float hv[2][32]; float am[2] = {0.f, 0.f};
; #pragma unroll
;             for (int u = 0; u < 2; ++u)
; #pragma unroll
;                 for (int w = 0; w < 4; ++w) { const v4u a = xn[u][w]; const int o = 8 * w;
;                     hv[u][o] = bflo(a.x); hv[u][o + 1] = bfhi(a.x); hv[u][o + 2] = bflo(a.y); hv[u][o + 3] = bfhi(a.y); hv[u][o + 4] = bflo(a.z); hv[u][o + 5] = bfhi(a.z); hv[u][o + 6] = bflo(a.w); hv[u][o + 7] = bfhi(a.w); }
;             if (p < 3) YQ_XLOAD(p + 1);
.LBB0_901:
	s_cmp_eq_u32 s29, 6
	s_mov_b32 s2, 6
	s_cbranch_scc1 .LBB0_903
	s_add_i32 s10, s15, s29
	s_add_i32 s2, s10, 2
	s_ashr_i32 s3, s2, 31
	s_lshl_b64 s[2:3], s[2:3], 12
	v_lshl_add_u64 v[10:11], v[66:67], 0, s[2:3]
	s_add_i32 s2, s10, 3
	s_ashr_i32 s3, s2, 31
	s_lshl_b64 s[2:3], s[2:3], 12
	v_lshl_add_u64 v[26:27], v[66:67], 0, s[2:3]
	global_load_dwordx4 v[6:9], v[10:11], off offset:16
	global_load_dwordx4 v[2:5], v[10:11], off
	global_load_dwordx4 v[14:17], v[10:11], off offset:2064
	s_nop 0
	global_load_dwordx4 v[10:13], v[10:11], off offset:2048
	s_nop 0
	global_load_dwordx4 v[22:25], v[26:27], off offset:16
	global_load_dwordx4 v[18:21], v[26:27], off
	global_load_dwordx4 v[30:33], v[26:27], off offset:2064
	s_nop 0
	global_load_dwordx4 v[26:29], v[26:27], off offset:2048
	s_mov_b32 s2, s29
